# final6 + loop-edge edits in both diff-attention loops: loop-carried increments moved ahead of end-of-step wait+barrier (back-edge rotation) and shortened no-rescale vote (s_cmp_eq_u64 vcc,exec -> exp
# speedup vs baseline: 1.0048x; 1.0048x over previous
; DI void attn_unit_diff(const Ctx& C, int l, int b, int h, int j) {
;     ...
;     for (int sd = 0; sd < nt; ++sd) {
;         const int slot = sd % 3;
;         const bool staged = sd + 2 < nt;
;         if (staged) at_stage1(C.lds, projb, kcolB, vcolB, sd + 2, (sd + 2) % 3, wid, lb0, lb1);
.Lrot_d1_inc:
	s_add_i32 s94, s94, 1
	s_add_i32 s49, s49, 0x8000
	s_add_i32 s48, s48, 64
	s_add_i32 s79, s79, 1
	v_add_u32_e32 v159, 0x100, v159
	v_lshl_add_u64 v[146:147], v[146:147], 0, s[68:69]
	v_lshl_add_u64 v[148:149], v[148:149], 0, s[68:69]
	v_lshl_add_u64 v[150:151], v[150:151], 0, s[68:69]
.LBB0_786:
	s_cmp_eq_u32 s95, s49
	s_cbranch_scc1 .LBB0_805

; DI float max_x32(float v, int lane) { return fmaxf(v, bpx(v, lane, 32)); }
; DI float at_softmax(f32x16& p0, f32x16& p1, float& m_run, bool first, bool nearb, LAS const float* tabp, int lane) {
;     ...
;     float mx = p0[0];
; #pragma unroll
;     for (int i = 1; i < 16; ++i) mx = fmaxf(mx, p0[i]);
; #pragma unroll
;     for (int i = 0; i < 16; ++i) mx = fmaxf(mx, p1[i]);
;     float alpha = 1.f;
;     if (first || !__all(mx <= AT_THR)) {
;         mx = max_x32(mx, lane);
;         const float dl = first ? mx : fmaxf(mx, 0.f);
;         alpha = first ? 1.f : __builtin_amdgcn_exp2f(-dl); m_run += dl;
; #pragma unroll
;         for (int i = 0; i < 16; ++i) { p0[i] -= dl; p1[i] -= dl; }
;     }
.LBB0_794:
	s_nop 9
	v_max_f32_e32 v0, v113, v113
	v_max_f32_e32 v2, v112, v112
	v_max_f32_e32 v0, v2, v0
	v_max3_f32 v0, v0, v114, v115
	v_max3_f32 v0, v0, v116, v117
	v_max3_f32 v0, v0, v118, v119
	v_max3_f32 v0, v0, v120, v121
	v_max3_f32 v0, v0, v122, v123
	v_max3_f32 v0, v0, v124, v125
	v_max3_f32 v0, v0, v126, v127
	v_max3_f32 v0, v0, v96, v97
	v_max3_f32 v0, v0, v98, v99
	v_max3_f32 v0, v0, v100, v101
	v_max3_f32 v0, v0, v102, v103
	v_max3_f32 v0, v0, v104, v105
	v_max3_f32 v0, v0, v106, v107
	s_xor_b64 s[58:59], s[38:39], -1
	v_max3_f32 v0, v0, v108, v109
	v_max3_f32 v2, v0, v110, v111
	s_and_b64 vcc, exec, s[58:59]
	s_cbranch_vccz .LBB0_796
	s_mov_b32 s58, 0x41000000
	v_cmp_ge_f32_e32 vcc, s58, v2
	s_cmp_eq_u64 vcc, exec
	s_cbranch_scc1 .LBB0_801
	s_cmp_lg_u64 vcc, exec
	s_cselect_b64 s[58:59], -1, 0
	s_cbranch_execz .LBB0_797
	s_branch .LBB0_798

; DI void attn_unit_diff(const Ctx& C, int l, int b, int h, int j) {
;     ...
;     for (int sd = 0; sd < nt; ++sd) {
;     ...
;         if (staged) asm volatile("s_waitcnt vmcnt(4) lgkmcnt(0)\n\ts_barrier" ::: "memory");
;         else        asm volatile("s_waitcnt vmcnt(0) lgkmcnt(0)\n\ts_barrier" ::: "memory");
;     }
.LBB0_802:
	s_add_i32 s94, s94, 1
	s_add_i32 s49, s49, 0x8000
	s_add_i32 s48, s48, 64
	s_add_i32 s79, s79, 1
	v_add_u32_e32 v159, 0x100, v159
	v_lshl_add_u64 v[146:147], v[146:147], 0, s[68:69]
	v_lshl_add_u64 v[148:149], v[148:149], 0, s[68:69]
	v_lshl_add_u64 v[150:151], v[150:151], 0, s[68:69]
	s_waitcnt vmcnt(0) lgkmcnt(0)
	s_barrier
	s_cbranch_execnz .LBB0_786
.LBB0_803:
	s_add_i32 s94, s94, 1
	s_add_i32 s49, s49, 0x8000
	s_add_i32 s48, s48, 64
	s_add_i32 s79, s79, 1
	v_add_u32_e32 v159, 0x100, v159
	v_lshl_add_u64 v[146:147], v[146:147], 0, s[68:69]
	v_lshl_add_u64 v[148:149], v[148:149], 0, s[68:69]
	v_lshl_add_u64 v[150:151], v[150:151], 0, s[68:69]
	s_waitcnt vmcnt(4) lgkmcnt(0)
	s_barrier
	s_branch .LBB0_786

; DI void attn_unit_diff(const Ctx& C, int l, int b, int h, int j) {
;     ...
;     for (int sd = 0; sd < nt; ++sd) {
;         const int slot = sd % 3;
;         const bool staged = sd + 2 < nt;
;         if (staged) at_stage1(C.lds, projb, kcolB, vcolB, sd + 2, (sd + 2) % 3, wid, lb0, lb1);
.Lrot_d2_inc:
	s_add_i32 s35, s35, 1
	s_add_i32 s31, s31, 0x8000
	s_add_i32 s28, s28, 64
	s_add_i32 s15, s15, 1
	v_add_u32_e32 v159, 0x100, v159
	v_lshl_add_u64 v[146:147], v[146:147], 0, s[68:69]
	v_lshl_add_u64 v[148:149], v[148:149], 0, s[68:69]
	v_lshl_add_u64 v[150:151], v[150:151], 0, s[68:69]
.LBB0_829:
	s_cmp_eq_u32 s11, s31
	s_cbranch_scc1 .LBB0_848

; DI float max_x32(float v, int lane) { return fmaxf(v, bpx(v, lane, 32)); }
; DI float at_softmax(f32x16& p0, f32x16& p1, float& m_run, bool first, bool nearb, LAS const float* tabp, int lane) {
;     ...
;     float mx = p0[0];
; #pragma unroll
;     for (int i = 1; i < 16; ++i) mx = fmaxf(mx, p0[i]);
; #pragma unroll
;     for (int i = 0; i < 16; ++i) mx = fmaxf(mx, p1[i]);
;     float alpha = 1.f;
;     if (first || !__all(mx <= AT_THR)) {
;         mx = max_x32(mx, lane);
;         const float dl = first ? mx : fmaxf(mx, 0.f);
;         alpha = first ? 1.f : __builtin_amdgcn_exp2f(-dl); m_run += dl;
; #pragma unroll
;         for (int i = 0; i < 16; ++i) { p0[i] -= dl; p1[i] -= dl; }
;     }
.LBB0_837:
	s_nop 9
	v_max_f32_e32 v0, v113, v113
	v_max_f32_e32 v2, v112, v112
	v_max_f32_e32 v0, v2, v0
	v_max3_f32 v0, v0, v114, v115
	v_max3_f32 v0, v0, v116, v117
	v_max3_f32 v0, v0, v118, v119
	v_max3_f32 v0, v0, v120, v121
	v_max3_f32 v0, v0, v122, v123
	v_max3_f32 v0, v0, v124, v125
	v_max3_f32 v0, v0, v126, v127
	v_max3_f32 v0, v0, v96, v97
	v_max3_f32 v0, v0, v98, v99
	v_max3_f32 v0, v0, v100, v101
	v_max3_f32 v0, v0, v102, v103
	v_max3_f32 v0, v0, v104, v105
	v_max3_f32 v0, v0, v106, v107
	s_xor_b64 s[58:59], s[42:43], -1
	v_max3_f32 v0, v0, v108, v109
	v_max3_f32 v2, v0, v110, v111
	s_and_b64 vcc, exec, s[58:59]
	s_cbranch_vccz .LBB0_839
	s_mov_b32 s49, 0x41000000
	v_cmp_ge_f32_e32 vcc, s49, v2
	s_cmp_eq_u64 vcc, exec
	s_cbranch_scc1 .LBB0_844
	s_cmp_lg_u64 vcc, exec
	s_cselect_b64 s[58:59], -1, 0
	s_cbranch_execz .LBB0_840
	s_branch .LBB0_841

; DI void attn_unit_diff(const Ctx& C, int l, int b, int h, int j) {
;     ...
;     for (int sd = 0; sd < nt; ++sd) {
;     ...
;         if (staged) asm volatile("s_waitcnt vmcnt(4) lgkmcnt(0)\n\ts_barrier" ::: "memory");
;         else        asm volatile("s_waitcnt vmcnt(0) lgkmcnt(0)\n\ts_barrier" ::: "memory");
;     }
.LBB0_845:
	s_add_i32 s35, s35, 1
	s_add_i32 s31, s31, 0x8000
	s_add_i32 s28, s28, 64
	s_add_i32 s15, s15, 1
	v_add_u32_e32 v159, 0x100, v159
	v_lshl_add_u64 v[146:147], v[146:147], 0, s[68:69]
	v_lshl_add_u64 v[148:149], v[148:149], 0, s[68:69]
	v_lshl_add_u64 v[150:151], v[150:151], 0, s[68:69]
	s_waitcnt vmcnt(0) lgkmcnt(0)
	s_barrier
	s_cbranch_execnz .LBB0_829
.LBB0_846:
	s_add_i32 s35, s35, 1
	s_add_i32 s31, s31, 0x8000
	s_add_i32 s28, s28, 64
	s_add_i32 s15, s15, 1
	v_add_u32_e32 v159, 0x100, v159
	v_lshl_add_u64 v[146:147], v[146:147], 0, s[68:69]
	v_lshl_add_u64 v[148:149], v[148:149], 0, s[68:69]
	v_lshl_add_u64 v[150:151], v[150:151], 0, s[68:69]
	s_waitcnt vmcnt(4) lgkmcnt(0)
	s_barrier
	s_branch .LBB0_829
